# P6: the converter half (wg>=128, early at the P5->P6 barrier) starts its accumulators from the x tile fetched while it waits; its epilogue only stores
# speedup vs baseline: 1.0038x; 1.0015x over previous
; __device__ __forceinline__ void xcd_barrier(const XcdBarrier& b) {
;     asm volatile("s_waitcnt vmcnt(0)" ::: "memory");
;     __syncthreads();
; __device__ __forceinline__ void phase6() { const Ctx c = make_ctx(); PHASE_PTRS;
;         pg8::Gemm g{mixed, D * 2}; pg8::PlainSched Sc; Sc.init(Wout, M, D, D, c.G, c.wg);
.LBB0_1024:
	v_readlane_b32 s0, v252, 0
	v_readlane_b32 s1, v252, 1
	s_cmp_lt_i32 s0, 6
	s_cselect_b64 s[6:7], -1, 0
	s_cmp_gt_i32 s1, 6
	s_cselect_b64 s[4:5], -1, 0
	s_and_b64 s[6:7], s[6:7], s[4:5]
	s_andn2_b64 vcc, exec, s[6:7]
	s_cbranch_vccnz .LBB0_1078
	s_waitcnt vmcnt(0)
	v_readlane_b32 s0, v252, 4
	v_readlane_b32 s1, v252, 5
	s_waitcnt vmcnt(0) lgkmcnt(0)
	s_barrier
	s_cmpk_gt_i32 s2, 0xff
	s_cbranch_scc1 .Lp6x_skip
	s_cmpk_lt_i32 s2, 0x80
	s_cbranch_scc1 .Lp6x_skip
	s_load_dwordx2 s[14:15], s[94:95], 0x0
	s_ashr_i32 s8, s2, 31
	s_lshr_b32 s8, s8, 29
	s_add_i32 s12, s2, s8
	s_and_b32 s8, s12, -8
	s_sub_i32 s10, s2, s8
	s_cmp_gt_i32 s10, -1
	s_cbranch_scc0 .Lp6x_neg
	s_lshl_b32 s11, s10, 5
	s_ashr_i32 s8, s12, 3
	s_branch .Lp6x_join

; template <class Epi, class Sched, bool ALIGN_EPI, bool FP8 = false>
; __device__ __forceinline__ void gemm_phase(LAS unsigned char* lds, const Gemm g, const Sched& S, const Epi& E) {
;     ...
;     const int tid = tid_, wid = __builtin_amdgcn_readfirstlane(tid >> 6), lane = tid & 63, wr = wid >> 2, wc = wid & 3, fr = lane & 15, fq = lane >> 4;
;     const int RB = g.RB, nt = RB / (BK * 2);
;     int sR[2], sC[2]; unsigned voffB[2];
; #pragma unroll
;     for (int i = 0; i < 2; ++i) { stage_rc(tid * 16 + i * 8192, sR[i], sC[i]); const int Rb = Epi::PERM ? ((sR[i] & ~31) + perm32(sR[i] & 31)) : sR[i]; voffB[i] = (unsigned)(Rb * RB + sC[i] * 2); }
;     const size_t kstep = (size_t)(BK * 2);
;     const size_t hstep = (size_t)HALF * RB;
;     const unsigned ldsw = (unsigned)wid * 1024u;
;     const int aoff = lds_byte(wr * 64 + fr, fq * 8), boff = lds_byte(wc * 32 + fr, fq * 8);
;     __device__ __forceinline__ void operator()(const f32x4 (&acc)[2][2][4][2], const Unit& u, int wr, int wc, int fr, int fq, const LAS float* bl) const {
;     ...
;             for (int m = 0; m < 4; ++m) { const size_t off = (size_t)(row0 + ai * HALF + m * 16) * ldc + col0;
; #pragma unroll
;                 for (int bj = 0; bj < 2; ++bj)
; #pragma unroll
;                     for (int n = 0; n < 2; ++n) res[m][bj][n] = __builtin_nontemporal_load((const f32x4*)(base + off + bj * HALF + n * 16)); }
.LBB0_1085:
	s_load_dwordx2 s[12:13], s[6:7], 0x0
	s_andn2_b64 vcc, exec, s[8:9]
	s_cbranch_vccnz .LBB0_1115
	v_readlane_b32 s98, v252, 0
	s_cmp_lt_i32 s98, 6
	s_cselect_b32 s98, 1, 0
	s_cmpk_gt_i32 s2, 0x7f
	s_cselect_b32 s98, s98, 0
	v_bfe_i32 v234, v1, 27, 1
	v_lshlrev_b32_e32 v232, 4, v1
	v_lshrrev_b32_e32 v234, 22, v234
	v_add_u32_e32 v234, v232, v234
	v_and_b32_e32 v234, 0xfffffc00, v234
	v_sub_u32_e32 v234, v232, v234
	v_lshrrev_b32_e32 v235, 4, v234
	v_bitop3_b32 v234, v235, v234, 32 bitop3:0x6c
	v_ashrrev_i32_e32 v236, 31, v234
	v_ashrrev_i32_e32 v233, 31, v1
	v_lshrrev_b32_e32 v236, 26, v236
	v_lshrrev_b32_e32 v233, 26, v233
	v_add_u32_e32 v236, v234, v236
	v_add_u32_e32 v233, v1, v233
	v_ashrrev_i32_e32 v237, 6, v236
	v_and_b32_e32 v236, 0xc0, v236
	v_ashrrev_i32_e32 v233, 6, v233
	v_sub_u32_e32 v234, v234, v236
	v_mov_b32_e32 v210, 1
	v_lshlrev_b32_e32 v235, 3, v233
	v_lshlrev_b32_e32 v233, 5, v233
	v_ashrrev_i16_sdwa v234, v210, sext(v234) dst_sel:DWORD dst_unused:UNUSED_PAD src0_sel:DWORD src1_sel:BYTE_0
	v_and_b32_e32 v233, 32, v233
	v_bfe_i32 v234, v234, 0, 16
	v_add_u32_e32 v232, 0x2000, v232
	v_add_lshl_u32 v233, v233, v234, 1
	v_ashrrev_i32_e32 v234, 31, v232
	v_lshrrev_b32_e32 v234, 22, v234
	v_add_u32_e32 v234, v232, v234
	v_ashrrev_i32_e32 v234, 10, v234
	v_mul_i32_i24_e32 v236, 0x400, v234
	v_sub_u32_e32 v232, v232, v236
	v_lshrrev_b32_e32 v236, 4, v232
	v_and_b32_e32 v235, -16, v235
	v_bitop3_b32 v232, v236, v232, 32 bitop3:0x6c
	v_add_u32_e32 v235, v237, v235
	v_ashrrev_i32_e32 v237, 31, v232
	v_lshrrev_b32_e32 v237, 26, v237
	v_add_u32_e32 v237, v232, v237
	s_waitcnt lgkmcnt(0)
	s_cmp_lt_u32 s40, 64
	s_cbranch_scc0 .Lp6x_w0done
	s_cmp_eq_u32 s98, 1
	s_cbranch_scc0 .Lp6x_w0done
	global_load_dwordx4 v[126:129], v244, s[12:13] nt
	global_load_dwordx4 v[122:125], v244, s[12:13] offset:64 nt
	global_load_dwordx4 v[114:117], v244, s[12:13] offset:512 nt
	global_load_dwordx4 v[106:109], v244, s[12:13] offset:576 nt
	global_load_dwordx4 v[118:121], v245, s[12:13] nt
	global_load_dwordx4 v[110:113], v245, s[12:13] offset:64 nt
	global_load_dwordx4 v[98:101], v245, s[12:13] offset:512 nt
	global_load_dwordx4 v[90:93], v245, s[12:13] offset:576 nt
	global_load_dwordx4 v[102:105], v246, s[12:13] nt
	global_load_dwordx4 v[94:97], v246, s[12:13] offset:64 nt
	global_load_dwordx4 v[82:85], v246, s[12:13] offset:512 nt
	global_load_dwordx4 v[78:81], v246, s[12:13] offset:576 nt
	global_load_dwordx4 v[86:89], v247, s[12:13] nt
	global_load_dwordx4 v[74:77], v247, s[12:13] offset:64 nt
	global_load_dwordx4 v[70:73], v247, s[12:13] offset:512 nt
	global_load_dwordx4 v[66:69], v247, s[12:13] offset:576 nt
	global_load_dwordx4 v[54:57], v248, s[12:13] nt
	global_load_dwordx4 v[50:53], v248, s[12:13] offset:64 nt
	global_load_dwordx4 v[42:45], v248, s[12:13] offset:512 nt
	global_load_dwordx4 v[34:37], v248, s[12:13] offset:576 nt
	global_load_dwordx4 v[46:49], v249, s[12:13] nt
	global_load_dwordx4 v[38:41], v249, s[12:13] offset:64 nt
	global_load_dwordx4 v[26:29], v249, s[12:13] offset:512 nt
	global_load_dwordx4 v[10:13], v249, s[12:13] offset:576 nt
	global_load_dwordx4 v[30:33], v250, s[12:13] nt
	global_load_dwordx4 v[18:21], v250, s[12:13] offset:64 nt
	global_load_dwordx4 v[62:65], v250, s[12:13] offset:512 nt
	global_load_dwordx4 v[58:61], v250, s[12:13] offset:576 nt
	global_load_dwordx4 v[14:17], v251, s[12:13] nt
	global_load_dwordx4 v[6:9], v251, s[12:13] offset:64 nt
	global_load_dwordx4 v[22:25], v251, s[12:13] offset:512 nt
	global_load_dwordx4 v[2:5], v251, s[12:13] offset:576 nt
